# KV2 loader waves: 3 register stages in flight instead of 4, on top of prep_all nt input loads
# baseline (speedup 1.0000x reference)
.LBB3_63:
	s_and_b64 vcc, exec, s[2:3]
	s_cbranch_vccz .LBB3_66
	v_add_u32_e32 v1, 0xffffff00, v0
	v_ashrrev_i32_e32 v74, 3, v1
	v_and_b32_e32 v4, 7, v0
	v_lshlrev_b32_e32 v4, 4, v4
	v_lshl_add_u32 v150, v74, 11, v4
	v_add_u32_e32 v151, 0x8000, v150
	v_add_u32_e32 v152, 0x10000, v150
	v_add_u32_e32 v153, 0x18000, v150
	v_add_u32_e32 v154, 0x20000, v150
	v_add_u32_e32 v155, 0x28000, v150
	v_add_u32_e32 v156, 0x30000, v150
	v_add_u32_e32 v157, 0x38000, v150
	v_lshlrev_b32_e32 v75, 4, v0
	global_load_dwordx4 v[2:5], v150, s[6:7]
	global_load_dwordx4 v[6:9], v151, s[6:7]
	global_load_dwordx4 v[10:13], v152, s[6:7]
	global_load_dwordx4 v[14:17], v153, s[6:7]
	global_load_dwordx4 v[18:21], v154, s[6:7]
	global_load_dwordx4 v[22:25], v155, s[6:7]
	global_load_dwordx4 v[26:29], v156, s[6:7]
	global_load_dwordx4 v[30:33], v157, s[6:7]
	global_load_dwordx4 v[34:37], v150, s[6:7] offset:128
	global_load_dwordx4 v[38:41], v151, s[6:7] offset:128
	global_load_dwordx4 v[42:45], v152, s[6:7] offset:128
	global_load_dwordx4 v[46:49], v153, s[6:7] offset:128
	global_load_dwordx4 v[50:53], v154, s[6:7] offset:128
	global_load_dwordx4 v[54:57], v155, s[6:7] offset:128
	global_load_dwordx4 v[58:61], v156, s[6:7] offset:128
	global_load_dwordx4 v[62:65], v157, s[6:7] offset:128
	global_load_dwordx4 v[84:87], v150, s[6:7] offset:256
	global_load_dwordx4 v[88:91], v151, s[6:7] offset:256
	global_load_dwordx4 v[92:95], v152, s[6:7] offset:256
	global_load_dwordx4 v[96:99], v153, s[6:7] offset:256
	global_load_dwordx4 v[100:103], v154, s[6:7] offset:256
	global_load_dwordx4 v[104:107], v155, s[6:7] offset:256
	global_load_dwordx4 v[108:111], v156, s[6:7] offset:256
	global_load_dwordx4 v[112:115], v157, s[6:7] offset:256
	v_bfe_u32 v76, v0, 2, 1
	v_lshrrev_b32_e32 v1, 6, v1
	s_mov_b32 s0, 0x3ffffe
	v_and_b32_e32 v75, 48, v75
	v_and_or_b32 v1, v1, s0, v76
	v_lshlrev_b32_e32 v68, 6, v74
	s_movk_i32 s1, 0x3c0
	v_lshlrev_b32_e32 v69, 2, v74
	v_and_or_b32 v68, v68, s1, v75
	v_lshlrev_b32_e32 v1, 10, v1
	v_and_b32_e32 v69, 32, v69
	v_bitop3_b32 v1, v68, v1, v69 bitop3:0xde
	v_add_u32_e32 v68, 16, v74
	v_lshrrev_b32_e32 v69, 3, v68
	v_and_or_b32 v69, v69, s0, v76
	v_lshlrev_b32_e32 v70, 6, v68
	v_lshlrev_b32_e32 v68, 2, v68
	v_and_or_b32 v70, v70, s1, v75
	v_lshlrev_b32_e32 v69, 10, v69
	v_and_b32_e32 v68, 32, v68
	v_bitop3_b32 v68, v70, v69, v68 bitop3:0xde
	v_add_u32_e32 v69, 32, v74
	v_lshrrev_b32_e32 v70, 3, v69
	v_and_or_b32 v70, v70, s0, v76
	v_lshlrev_b32_e32 v71, 6, v69
	v_lshlrev_b32_e32 v69, 2, v69
	v_and_or_b32 v71, v71, s1, v75
	v_lshlrev_b32_e32 v70, 10, v70
	v_and_b32_e32 v69, 32, v69
	v_bitop3_b32 v69, v71, v70, v69 bitop3:0xde
	v_add_u32_e32 v70, 48, v74
	v_lshrrev_b32_e32 v71, 3, v70
	v_and_or_b32 v71, v71, s0, v76
	v_lshlrev_b32_e32 v72, 6, v70
	v_lshlrev_b32_e32 v70, 2, v70
	v_and_or_b32 v72, v72, s1, v75
	v_lshlrev_b32_e32 v71, 10, v71
	v_and_b32_e32 v70, 32, v70
	v_bitop3_b32 v70, v72, v71, v70 bitop3:0xde
	v_add_u32_e32 v71, 64, v74
	v_lshrrev_b32_e32 v72, 3, v71
	v_and_or_b32 v72, v72, s0, v76
	v_lshlrev_b32_e32 v73, 6, v71
	v_lshlrev_b32_e32 v71, 2, v71
	v_and_or_b32 v73, v73, s1, v75
	v_lshlrev_b32_e32 v72, 10, v72
	v_and_b32_e32 v71, 32, v71
	v_bitop3_b32 v71, v73, v72, v71 bitop3:0xde
	v_add_u32_e32 v72, 0x50, v74
	v_lshrrev_b32_e32 v73, 3, v72
	v_and_or_b32 v73, v73, s0, v76
	v_lshlrev_b32_e32 v77, 6, v72
	v_lshlrev_b32_e32 v72, 2, v72
	v_and_or_b32 v77, v77, s1, v75
	v_lshlrev_b32_e32 v73, 10, v73
	v_and_b32_e32 v72, 32, v72
	v_bitop3_b32 v72, v77, v73, v72 bitop3:0xde
	v_add_u32_e32 v73, 0x60, v74
	v_lshrrev_b32_e32 v77, 3, v73
	v_and_or_b32 v77, v77, s0, v76
	v_lshlrev_b32_e32 v78, 6, v73
	v_lshlrev_b32_e32 v73, 2, v73
	v_and_or_b32 v78, v78, s1, v75
	v_lshlrev_b32_e32 v77, 10, v77
	v_and_b32_e32 v73, 32, v73
	v_add_u32_e32 v74, 0x70, v74
	v_bitop3_b32 v73, v78, v77, v73 bitop3:0xde
	v_lshrrev_b32_e32 v77, 3, v74
	v_and_or_b32 v76, v77, s0, v76
	v_lshlrev_b32_e32 v77, 6, v74
	v_lshlrev_b32_e32 v74, 2, v74
	v_and_or_b32 v75, v77, s1, v75
	v_lshlrev_b32_e32 v76, 10, v76
	v_and_b32_e32 v74, 32, v74
	v_bitop3_b32 v74, v75, v76, v74 bitop3:0xde
	s_waitcnt vmcnt(16)
	ds_write_b128 v1, v[2:5]
	ds_write_b128 v68, v[6:9]
	ds_write_b128 v69, v[10:13]
	ds_write_b128 v70, v[14:17]
	ds_write_b128 v71, v[18:21]
	ds_write_b128 v72, v[22:25]
	ds_write_b128 v73, v[26:29]
	ds_write_b128 v74, v[30:33]
	global_load_dwordx4 v[2:5], v150, s[6:7] offset:384
	global_load_dwordx4 v[6:9], v151, s[6:7] offset:384
	global_load_dwordx4 v[10:13], v152, s[6:7] offset:384
	global_load_dwordx4 v[14:17], v153, s[6:7] offset:384
	global_load_dwordx4 v[18:21], v154, s[6:7] offset:384
	global_load_dwordx4 v[22:25], v155, s[6:7] offset:384
	global_load_dwordx4 v[26:29], v156, s[6:7] offset:384
	global_load_dwordx4 v[30:33], v157, s[6:7] offset:384
	s_waitcnt lgkmcnt(0)
	s_barrier
	s_waitcnt vmcnt(16)
	ds_write_b128 v1, v[34:37] offset:24576
	ds_write_b128 v68, v[38:41] offset:24576
	ds_write_b128 v69, v[42:45] offset:24576
	ds_write_b128 v70, v[46:49] offset:24576
	ds_write_b128 v71, v[50:53] offset:24576
	ds_write_b128 v72, v[54:57] offset:24576
	ds_write_b128 v73, v[58:61] offset:24576
	ds_write_b128 v74, v[62:65] offset:24576
	global_load_dwordx4 v[34:37], v150, s[6:7] offset:512
	global_load_dwordx4 v[38:41], v151, s[6:7] offset:512
	global_load_dwordx4 v[42:45], v152, s[6:7] offset:512
	global_load_dwordx4 v[46:49], v153, s[6:7] offset:512
	global_load_dwordx4 v[50:53], v154, s[6:7] offset:512
	global_load_dwordx4 v[54:57], v155, s[6:7] offset:512
	global_load_dwordx4 v[58:61], v156, s[6:7] offset:512
	global_load_dwordx4 v[62:65], v157, s[6:7] offset:512
	s_waitcnt lgkmcnt(0)
	s_barrier
	s_waitcnt vmcnt(16)
	ds_write_b128 v1, v[84:87] offset:49152
	ds_write_b128 v68, v[88:91] offset:49152
	ds_write_b128 v69, v[92:95] offset:49152
	ds_write_b128 v70, v[96:99] offset:49152
	ds_write_b128 v71, v[100:103] offset:49152
	ds_write_b128 v72, v[104:107] offset:49152
	ds_write_b128 v73, v[108:111] offset:49152
	ds_write_b128 v74, v[112:115] offset:49152
	global_load_dwordx4 v[84:87], v150, s[6:7] offset:640
	global_load_dwordx4 v[88:91], v151, s[6:7] offset:640
	global_load_dwordx4 v[92:95], v152, s[6:7] offset:640
	global_load_dwordx4 v[96:99], v153, s[6:7] offset:640
	global_load_dwordx4 v[100:103], v154, s[6:7] offset:640
	global_load_dwordx4 v[104:107], v155, s[6:7] offset:640
	global_load_dwordx4 v[108:111], v156, s[6:7] offset:640
	global_load_dwordx4 v[112:115], v157, s[6:7] offset:640
	s_waitcnt lgkmcnt(0)
	s_barrier
	s_waitcnt vmcnt(16)
	ds_write_b128 v1, v[2:5]
	ds_write_b128 v68, v[6:9]
	ds_write_b128 v69, v[10:13]
	ds_write_b128 v70, v[14:17]
	ds_write_b128 v71, v[18:21]
	ds_write_b128 v72, v[22:25]
	ds_write_b128 v73, v[26:29]
	ds_write_b128 v74, v[30:33]
	global_load_dwordx4 v[2:5], v150, s[6:7] offset:768
	global_load_dwordx4 v[6:9], v151, s[6:7] offset:768
	global_load_dwordx4 v[10:13], v152, s[6:7] offset:768
	global_load_dwordx4 v[14:17], v153, s[6:7] offset:768
	global_load_dwordx4 v[18:21], v154, s[6:7] offset:768
	global_load_dwordx4 v[22:25], v155, s[6:7] offset:768
	global_load_dwordx4 v[26:29], v156, s[6:7] offset:768
	global_load_dwordx4 v[30:33], v157, s[6:7] offset:768
	s_waitcnt lgkmcnt(0)
	s_barrier
	s_waitcnt vmcnt(16)
	ds_write_b128 v1, v[34:37] offset:24576
	ds_write_b128 v68, v[38:41] offset:24576
	ds_write_b128 v69, v[42:45] offset:24576
	ds_write_b128 v70, v[46:49] offset:24576
	ds_write_b128 v71, v[50:53] offset:24576
	ds_write_b128 v72, v[54:57] offset:24576
	ds_write_b128 v73, v[58:61] offset:24576
	ds_write_b128 v74, v[62:65] offset:24576
	global_load_dwordx4 v[34:37], v150, s[6:7] offset:896
	global_load_dwordx4 v[38:41], v151, s[6:7] offset:896
	global_load_dwordx4 v[42:45], v152, s[6:7] offset:896
	global_load_dwordx4 v[46:49], v153, s[6:7] offset:896
	global_load_dwordx4 v[50:53], v154, s[6:7] offset:896
	global_load_dwordx4 v[54:57], v155, s[6:7] offset:896
	global_load_dwordx4 v[58:61], v156, s[6:7] offset:896
	global_load_dwordx4 v[62:65], v157, s[6:7] offset:896
	s_waitcnt lgkmcnt(0)
	s_barrier
	s_waitcnt vmcnt(16)
	ds_write_b128 v1, v[84:87] offset:49152
	ds_write_b128 v68, v[88:91] offset:49152
	ds_write_b128 v69, v[92:95] offset:49152
	ds_write_b128 v70, v[96:99] offset:49152
	ds_write_b128 v71, v[100:103] offset:49152
	ds_write_b128 v72, v[104:107] offset:49152
	ds_write_b128 v73, v[108:111] offset:49152
	ds_write_b128 v74, v[112:115] offset:49152
	global_load_dwordx4 v[84:87], v150, s[6:7] offset:1024
	global_load_dwordx4 v[88:91], v151, s[6:7] offset:1024
	global_load_dwordx4 v[92:95], v152, s[6:7] offset:1024
	global_load_dwordx4 v[96:99], v153, s[6:7] offset:1024
	global_load_dwordx4 v[100:103], v154, s[6:7] offset:1024
	global_load_dwordx4 v[104:107], v155, s[6:7] offset:1024
	global_load_dwordx4 v[108:111], v156, s[6:7] offset:1024
	global_load_dwordx4 v[112:115], v157, s[6:7] offset:1024
	s_waitcnt lgkmcnt(0)
	s_barrier
	s_waitcnt vmcnt(16)
	ds_write_b128 v1, v[2:5]
	ds_write_b128 v68, v[6:9]
	ds_write_b128 v69, v[10:13]
	ds_write_b128 v70, v[14:17]
	ds_write_b128 v71, v[18:21]
	ds_write_b128 v72, v[22:25]
	ds_write_b128 v73, v[26:29]
	ds_write_b128 v74, v[30:33]
	global_load_dwordx4 v[2:5], v150, s[6:7] offset:1152
	global_load_dwordx4 v[6:9], v151, s[6:7] offset:1152
	global_load_dwordx4 v[10:13], v152, s[6:7] offset:1152
	global_load_dwordx4 v[14:17], v153, s[6:7] offset:1152
	global_load_dwordx4 v[18:21], v154, s[6:7] offset:1152
	global_load_dwordx4 v[22:25], v155, s[6:7] offset:1152
	global_load_dwordx4 v[26:29], v156, s[6:7] offset:1152
	global_load_dwordx4 v[30:33], v157, s[6:7] offset:1152
	s_waitcnt lgkmcnt(0)
	s_barrier
	s_waitcnt vmcnt(16)
	ds_write_b128 v1, v[34:37] offset:24576
	ds_write_b128 v68, v[38:41] offset:24576
	ds_write_b128 v69, v[42:45] offset:24576
	ds_write_b128 v70, v[46:49] offset:24576
	ds_write_b128 v71, v[50:53] offset:24576
	ds_write_b128 v72, v[54:57] offset:24576
	ds_write_b128 v73, v[58:61] offset:24576
	ds_write_b128 v74, v[62:65] offset:24576
	global_load_dwordx4 v[34:37], v150, s[6:7] offset:1280
	global_load_dwordx4 v[38:41], v151, s[6:7] offset:1280
	global_load_dwordx4 v[42:45], v152, s[6:7] offset:1280
	global_load_dwordx4 v[46:49], v153, s[6:7] offset:1280
	global_load_dwordx4 v[50:53], v154, s[6:7] offset:1280
	global_load_dwordx4 v[54:57], v155, s[6:7] offset:1280
	global_load_dwordx4 v[58:61], v156, s[6:7] offset:1280
	global_load_dwordx4 v[62:65], v157, s[6:7] offset:1280
	s_waitcnt lgkmcnt(0)
	s_barrier
	s_waitcnt vmcnt(16)
	ds_write_b128 v1, v[84:87] offset:49152
	ds_write_b128 v68, v[88:91] offset:49152
	ds_write_b128 v69, v[92:95] offset:49152
	ds_write_b128 v70, v[96:99] offset:49152
	ds_write_b128 v71, v[100:103] offset:49152
	ds_write_b128 v72, v[104:107] offset:49152
	ds_write_b128 v73, v[108:111] offset:49152
	ds_write_b128 v74, v[112:115] offset:49152
	global_load_dwordx4 v[84:87], v150, s[6:7] offset:1408
	global_load_dwordx4 v[88:91], v151, s[6:7] offset:1408
	global_load_dwordx4 v[92:95], v152, s[6:7] offset:1408
	global_load_dwordx4 v[96:99], v153, s[6:7] offset:1408
	global_load_dwordx4 v[100:103], v154, s[6:7] offset:1408
	global_load_dwordx4 v[104:107], v155, s[6:7] offset:1408
	global_load_dwordx4 v[108:111], v156, s[6:7] offset:1408
	global_load_dwordx4 v[112:115], v157, s[6:7] offset:1408
	s_waitcnt lgkmcnt(0)
	s_barrier
	s_waitcnt vmcnt(16)
	ds_write_b128 v1, v[2:5]
	ds_write_b128 v68, v[6:9]
	ds_write_b128 v69, v[10:13]
	ds_write_b128 v70, v[14:17]
	ds_write_b128 v71, v[18:21]
	ds_write_b128 v72, v[22:25]
	ds_write_b128 v73, v[26:29]
	ds_write_b128 v74, v[30:33]
	global_load_dwordx4 v[2:5], v150, s[6:7] offset:1536
	global_load_dwordx4 v[6:9], v151, s[6:7] offset:1536
	global_load_dwordx4 v[10:13], v152, s[6:7] offset:1536
	global_load_dwordx4 v[14:17], v153, s[6:7] offset:1536
	global_load_dwordx4 v[18:21], v154, s[6:7] offset:1536
	global_load_dwordx4 v[22:25], v155, s[6:7] offset:1536
	global_load_dwordx4 v[26:29], v156, s[6:7] offset:1536
	global_load_dwordx4 v[30:33], v157, s[6:7] offset:1536
	s_waitcnt lgkmcnt(0)
	s_barrier
	s_waitcnt vmcnt(16)
	ds_write_b128 v1, v[34:37] offset:24576
	ds_write_b128 v68, v[38:41] offset:24576
	ds_write_b128 v69, v[42:45] offset:24576
	ds_write_b128 v70, v[46:49] offset:24576
	ds_write_b128 v71, v[50:53] offset:24576
	ds_write_b128 v72, v[54:57] offset:24576
	ds_write_b128 v73, v[58:61] offset:24576
	ds_write_b128 v74, v[62:65] offset:24576
	global_load_dwordx4 v[34:37], v150, s[6:7] offset:1664
	global_load_dwordx4 v[38:41], v151, s[6:7] offset:1664
	global_load_dwordx4 v[42:45], v152, s[6:7] offset:1664
	global_load_dwordx4 v[46:49], v153, s[6:7] offset:1664
	global_load_dwordx4 v[50:53], v154, s[6:7] offset:1664
	global_load_dwordx4 v[54:57], v155, s[6:7] offset:1664
	global_load_dwordx4 v[58:61], v156, s[6:7] offset:1664
	global_load_dwordx4 v[62:65], v157, s[6:7] offset:1664
	s_waitcnt lgkmcnt(0)
	s_barrier
	s_waitcnt vmcnt(16)
	ds_write_b128 v1, v[84:87] offset:49152
	ds_write_b128 v68, v[88:91] offset:49152
	ds_write_b128 v69, v[92:95] offset:49152
	ds_write_b128 v70, v[96:99] offset:49152
	ds_write_b128 v71, v[100:103] offset:49152
	ds_write_b128 v72, v[104:107] offset:49152
	ds_write_b128 v73, v[108:111] offset:49152
	ds_write_b128 v74, v[112:115] offset:49152
	global_load_dwordx4 v[84:87], v150, s[6:7] offset:1792
	global_load_dwordx4 v[88:91], v151, s[6:7] offset:1792
	global_load_dwordx4 v[92:95], v152, s[6:7] offset:1792
	global_load_dwordx4 v[96:99], v153, s[6:7] offset:1792
	global_load_dwordx4 v[100:103], v154, s[6:7] offset:1792
	global_load_dwordx4 v[104:107], v155, s[6:7] offset:1792
	global_load_dwordx4 v[108:111], v156, s[6:7] offset:1792
	global_load_dwordx4 v[112:115], v157, s[6:7] offset:1792
	s_waitcnt lgkmcnt(0)
	s_barrier
	s_waitcnt vmcnt(16)
	ds_write_b128 v1, v[2:5]
	ds_write_b128 v68, v[6:9]
	ds_write_b128 v69, v[10:13]
	ds_write_b128 v70, v[14:17]
	ds_write_b128 v71, v[18:21]
	ds_write_b128 v72, v[22:25]
	ds_write_b128 v73, v[26:29]
	ds_write_b128 v74, v[30:33]
	global_load_dwordx4 v[2:5], v150, s[6:7] offset:1920
	global_load_dwordx4 v[6:9], v151, s[6:7] offset:1920
	global_load_dwordx4 v[10:13], v152, s[6:7] offset:1920
	global_load_dwordx4 v[14:17], v153, s[6:7] offset:1920
	global_load_dwordx4 v[18:21], v154, s[6:7] offset:1920
	global_load_dwordx4 v[22:25], v155, s[6:7] offset:1920
	global_load_dwordx4 v[26:29], v156, s[6:7] offset:1920
	global_load_dwordx4 v[30:33], v157, s[6:7] offset:1920
	s_waitcnt lgkmcnt(0)
	s_barrier
	s_waitcnt vmcnt(16)
	ds_write_b128 v1, v[34:37] offset:24576
	ds_write_b128 v68, v[38:41] offset:24576
	ds_write_b128 v69, v[42:45] offset:24576
	ds_write_b128 v70, v[46:49] offset:24576
	ds_write_b128 v71, v[50:53] offset:24576
	ds_write_b128 v72, v[54:57] offset:24576
	ds_write_b128 v73, v[58:61] offset:24576
	ds_write_b128 v74, v[62:65] offset:24576
	s_waitcnt lgkmcnt(0)
	s_barrier
	s_waitcnt vmcnt(8)
	ds_write_b128 v1, v[84:87] offset:49152
	ds_write_b128 v68, v[88:91] offset:49152
	ds_write_b128 v69, v[92:95] offset:49152
	ds_write_b128 v70, v[96:99] offset:49152
	ds_write_b128 v71, v[100:103] offset:49152
	ds_write_b128 v72, v[104:107] offset:49152
	ds_write_b128 v73, v[108:111] offset:49152
	ds_write_b128 v74, v[112:115] offset:49152
	s_waitcnt lgkmcnt(0)
	s_barrier
	s_waitcnt vmcnt(0)
	ds_write_b128 v1, v[2:5]
	ds_write_b128 v68, v[6:9]
	ds_write_b128 v69, v[10:13]
	ds_write_b128 v70, v[14:17]
	ds_write_b128 v71, v[18:21]
	ds_write_b128 v72, v[22:25]
	ds_write_b128 v73, v[26:29]
	ds_write_b128 v74, v[30:33]
	s_waitcnt lgkmcnt(0)
	s_barrier

.LBB3_67:
	v_add_u32_e32 v1, 0xfffffe80, v0
	s_lshl_b32 s0, s24, 17
	v_ashrrev_i32_e32 v36, 3, v1
	s_add_u32 s28, s4, s0
	s_addc_u32 s29, s5, 0
	v_and_b32_e32 v4, 7, v0
	v_lshlrev_b32_e32 v4, 4, v4
	v_lshl_add_u32 v150, v36, 11, v4
	v_add_u32_e32 v151, 0x8000, v150
	v_add_u32_e32 v152, 0x10000, v150
	v_add_u32_e32 v153, 0x18000, v150
	v_lshlrev_b32_e32 v37, 4, v0
	global_load_dwordx4 v[2:5], v150, s[28:29]
	global_load_dwordx4 v[6:9], v151, s[28:29]
	global_load_dwordx4 v[10:13], v152, s[28:29]
	global_load_dwordx4 v[14:17], v153, s[28:29]
	global_load_dwordx4 v[18:21], v150, s[28:29] offset:128
	global_load_dwordx4 v[22:25], v151, s[28:29] offset:128
	global_load_dwordx4 v[26:29], v152, s[28:29] offset:128
	global_load_dwordx4 v[30:33], v153, s[28:29] offset:128
	global_load_dwordx4 v[50:53], v150, s[28:29] offset:256
	global_load_dwordx4 v[54:57], v151, s[28:29] offset:256
	global_load_dwordx4 v[58:61], v152, s[28:29] offset:256
	global_load_dwordx4 v[62:65], v153, s[28:29] offset:256
	v_lshlrev_b32_e32 v38, 6, v36
	v_lshlrev_b32_e32 v39, 2, v36
	v_add_u32_e32 v40, 16, v36
	v_add_u32_e32 v43, 32, v36
	v_add_u32_e32 v36, 48, v36
	v_bfe_u32 v0, v0, 2, 1
	v_lshrrev_b32_e32 v1, 6, v1
	s_mov_b32 s0, 0x3ffffe
	v_lshrrev_b32_e32 v41, 3, v40
	v_lshrrev_b32_e32 v44, 3, v43
	v_lshrrev_b32_e32 v46, 3, v36
	v_and_b32_e32 v37, 48, v37
	v_and_or_b32 v1, v1, s0, v0
	s_movk_i32 s5, 0x3c0
	v_and_or_b32 v41, v41, s0, v0
	v_lshlrev_b32_e32 v42, 6, v40
	v_and_or_b32 v44, v44, s0, v0
	v_lshlrev_b32_e32 v45, 6, v43
	v_and_or_b32 v0, v46, s0, v0
	v_lshlrev_b32_e32 v46, 6, v36
	v_and_or_b32 v38, v38, s5, v37
	v_and_or_b32 v42, v42, s5, v37
	v_lshlrev_b32_e32 v40, 2, v40
	v_and_or_b32 v45, v45, s5, v37
	v_lshlrev_b32_e32 v43, 2, v43
	v_and_or_b32 v37, v46, s5, v37
	v_lshlrev_b32_e32 v46, 10, v0
	v_lshlrev_b32_e32 v0, 2, v36
	v_lshlrev_b32_e32 v1, 10, v1
	v_and_b32_e32 v39, 32, v39
	v_lshlrev_b32_e32 v41, 10, v41
	v_and_b32_e32 v40, 32, v40
	v_lshlrev_b32_e32 v44, 10, v44
	v_and_b32_e32 v43, 32, v43
	v_and_b32_e32 v47, 32, v0
	s_mov_b32 s1, 0
	v_bitop3_b32 v0, v1, v38, v39 bitop3:0xf6
	v_bitop3_b32 v1, v41, v42, v40 bitop3:0xf6
	v_bitop3_b32 v36, v44, v45, v43 bitop3:0xf6
	v_bitop3_b32 v37, v46, v37, v47 bitop3:0xf6
	v_add_u32_e32 v0, 0x4000, v0
	v_add_u32_e32 v1, 0x4000, v1
	v_add_u32_e32 v36, 0x4000, v36
	v_add_u32_e32 v37, 0x4000, v37
	s_waitcnt vmcnt(8)
	ds_write_b128 v0, v[2:5]
	ds_write_b128 v1, v[6:9]
	ds_write_b128 v36, v[10:13]
	ds_write_b128 v37, v[14:17]
	global_load_dwordx4 v[2:5], v150, s[28:29] offset:384
	global_load_dwordx4 v[6:9], v151, s[28:29] offset:384
	global_load_dwordx4 v[10:13], v152, s[28:29] offset:384
	global_load_dwordx4 v[14:17], v153, s[28:29] offset:384
	s_waitcnt lgkmcnt(0)
	s_barrier
	s_waitcnt vmcnt(8)
	ds_write_b128 v0, v[18:21] offset:24576
	ds_write_b128 v1, v[22:25] offset:24576
	ds_write_b128 v36, v[26:29] offset:24576
	ds_write_b128 v37, v[30:33] offset:24576
	global_load_dwordx4 v[18:21], v150, s[28:29] offset:512
	global_load_dwordx4 v[22:25], v151, s[28:29] offset:512
	global_load_dwordx4 v[26:29], v152, s[28:29] offset:512
	global_load_dwordx4 v[30:33], v153, s[28:29] offset:512
	s_waitcnt lgkmcnt(0)
	s_barrier
	s_waitcnt vmcnt(8)
	ds_write_b128 v0, v[50:53] offset:49152
	ds_write_b128 v1, v[54:57] offset:49152
	ds_write_b128 v36, v[58:61] offset:49152
	ds_write_b128 v37, v[62:65] offset:49152
	global_load_dwordx4 v[50:53], v150, s[28:29] offset:640
	global_load_dwordx4 v[54:57], v151, s[28:29] offset:640
	global_load_dwordx4 v[58:61], v152, s[28:29] offset:640
	global_load_dwordx4 v[62:65], v153, s[28:29] offset:640
	s_waitcnt lgkmcnt(0)
	s_barrier
	s_waitcnt vmcnt(8)
	ds_write_b128 v0, v[2:5]
	ds_write_b128 v1, v[6:9]
	ds_write_b128 v36, v[10:13]
	ds_write_b128 v37, v[14:17]
	global_load_dwordx4 v[2:5], v150, s[28:29] offset:768
	global_load_dwordx4 v[6:9], v151, s[28:29] offset:768
	global_load_dwordx4 v[10:13], v152, s[28:29] offset:768
	global_load_dwordx4 v[14:17], v153, s[28:29] offset:768
	s_waitcnt lgkmcnt(0)
	s_barrier
	s_waitcnt vmcnt(8)
	ds_write_b128 v0, v[18:21] offset:24576
	ds_write_b128 v1, v[22:25] offset:24576
	ds_write_b128 v36, v[26:29] offset:24576
	ds_write_b128 v37, v[30:33] offset:24576
	global_load_dwordx4 v[18:21], v150, s[28:29] offset:896
	global_load_dwordx4 v[22:25], v151, s[28:29] offset:896
	global_load_dwordx4 v[26:29], v152, s[28:29] offset:896
	global_load_dwordx4 v[30:33], v153, s[28:29] offset:896
	s_waitcnt lgkmcnt(0)
	s_barrier
	s_waitcnt vmcnt(8)
	ds_write_b128 v0, v[50:53] offset:49152
	ds_write_b128 v1, v[54:57] offset:49152
	ds_write_b128 v36, v[58:61] offset:49152
	ds_write_b128 v37, v[62:65] offset:49152
	global_load_dwordx4 v[50:53], v150, s[28:29] offset:1024
	global_load_dwordx4 v[54:57], v151, s[28:29] offset:1024
	global_load_dwordx4 v[58:61], v152, s[28:29] offset:1024
	global_load_dwordx4 v[62:65], v153, s[28:29] offset:1024
	s_waitcnt lgkmcnt(0)
	s_barrier
	s_waitcnt vmcnt(8)
	ds_write_b128 v0, v[2:5]
	ds_write_b128 v1, v[6:9]
	ds_write_b128 v36, v[10:13]
	ds_write_b128 v37, v[14:17]
	global_load_dwordx4 v[2:5], v150, s[28:29] offset:1152
	global_load_dwordx4 v[6:9], v151, s[28:29] offset:1152
	global_load_dwordx4 v[10:13], v152, s[28:29] offset:1152
	global_load_dwordx4 v[14:17], v153, s[28:29] offset:1152
	s_waitcnt lgkmcnt(0)
	s_barrier
	s_waitcnt vmcnt(8)
	ds_write_b128 v0, v[18:21] offset:24576
	ds_write_b128 v1, v[22:25] offset:24576
	ds_write_b128 v36, v[26:29] offset:24576
	ds_write_b128 v37, v[30:33] offset:24576
	global_load_dwordx4 v[18:21], v150, s[28:29] offset:1280
	global_load_dwordx4 v[22:25], v151, s[28:29] offset:1280
	global_load_dwordx4 v[26:29], v152, s[28:29] offset:1280
	global_load_dwordx4 v[30:33], v153, s[28:29] offset:1280
	s_waitcnt lgkmcnt(0)
	s_barrier
	s_waitcnt vmcnt(8)
	ds_write_b128 v0, v[50:53] offset:49152
	ds_write_b128 v1, v[54:57] offset:49152
	ds_write_b128 v36, v[58:61] offset:49152
	ds_write_b128 v37, v[62:65] offset:49152
	global_load_dwordx4 v[50:53], v150, s[28:29] offset:1408
	global_load_dwordx4 v[54:57], v151, s[28:29] offset:1408
	global_load_dwordx4 v[58:61], v152, s[28:29] offset:1408
	global_load_dwordx4 v[62:65], v153, s[28:29] offset:1408
	s_waitcnt lgkmcnt(0)
	s_barrier
	s_waitcnt vmcnt(8)
	ds_write_b128 v0, v[2:5]
	ds_write_b128 v1, v[6:9]
	ds_write_b128 v36, v[10:13]
	ds_write_b128 v37, v[14:17]
	global_load_dwordx4 v[2:5], v150, s[28:29] offset:1536
	global_load_dwordx4 v[6:9], v151, s[28:29] offset:1536
	global_load_dwordx4 v[10:13], v152, s[28:29] offset:1536
	global_load_dwordx4 v[14:17], v153, s[28:29] offset:1536
	s_waitcnt lgkmcnt(0)
	s_barrier
	s_waitcnt vmcnt(8)
	ds_write_b128 v0, v[18:21] offset:24576
	ds_write_b128 v1, v[22:25] offset:24576
	ds_write_b128 v36, v[26:29] offset:24576
	ds_write_b128 v37, v[30:33] offset:24576
	global_load_dwordx4 v[18:21], v150, s[28:29] offset:1664
	global_load_dwordx4 v[22:25], v151, s[28:29] offset:1664
	global_load_dwordx4 v[26:29], v152, s[28:29] offset:1664
	global_load_dwordx4 v[30:33], v153, s[28:29] offset:1664
	s_waitcnt lgkmcnt(0)
	s_barrier
	s_waitcnt vmcnt(8)
	ds_write_b128 v0, v[50:53] offset:49152
	ds_write_b128 v1, v[54:57] offset:49152
	ds_write_b128 v36, v[58:61] offset:49152
	ds_write_b128 v37, v[62:65] offset:49152
	global_load_dwordx4 v[50:53], v150, s[28:29] offset:1792
	global_load_dwordx4 v[54:57], v151, s[28:29] offset:1792
	global_load_dwordx4 v[58:61], v152, s[28:29] offset:1792
	global_load_dwordx4 v[62:65], v153, s[28:29] offset:1792
	s_waitcnt lgkmcnt(0)
	s_barrier
	s_waitcnt vmcnt(8)
	ds_write_b128 v0, v[2:5]
	ds_write_b128 v1, v[6:9]
	ds_write_b128 v36, v[10:13]
	ds_write_b128 v37, v[14:17]
	global_load_dwordx4 v[2:5], v150, s[28:29] offset:1920
	global_load_dwordx4 v[6:9], v151, s[28:29] offset:1920
	global_load_dwordx4 v[10:13], v152, s[28:29] offset:1920
	global_load_dwordx4 v[14:17], v153, s[28:29] offset:1920
	s_waitcnt lgkmcnt(0)
	s_barrier
	s_waitcnt vmcnt(8)
	ds_write_b128 v0, v[18:21] offset:24576
	ds_write_b128 v1, v[22:25] offset:24576
	ds_write_b128 v36, v[26:29] offset:24576
	ds_write_b128 v37, v[30:33] offset:24576
	s_waitcnt lgkmcnt(0)
	s_barrier
	s_waitcnt vmcnt(4)
	ds_write_b128 v0, v[50:53] offset:49152
	ds_write_b128 v1, v[54:57] offset:49152
	ds_write_b128 v36, v[58:61] offset:49152
	ds_write_b128 v37, v[62:65] offset:49152
	s_waitcnt lgkmcnt(0)
	s_barrier
	s_waitcnt vmcnt(0)
	ds_write_b128 v0, v[2:5]
	ds_write_b128 v1, v[6:9]
	ds_write_b128 v36, v[10:13]
	ds_write_b128 v37, v[14:17]
	s_waitcnt lgkmcnt(0)
	s_barrier
